# v11 + ml_scan per-step gate scalars loaded once per unit and broadcast with v_readlane
# baseline (speedup 1.0000x reference)
.LBB0_785:
	s_ashr_i32 s8, s61, 3
	s_and_b32 s10, s61, 7
	s_mul_i32 s14, s8, 0x240
	s_mul_hi_i32 s9, s8, 0x240
	s_add_u32 s62, s55, s14
	s_addc_u32 s63, s56, s9
	v_min_u32_e32 v250, 35, v164
	v_lshlrev_b32_e32 v250, 4, v250
	global_load_dwordx2 v[248:249], v250, s[62:63]
	s_mul_hi_i32 s9, s8, 0x91200
	s_mul_i32 s8, s8, 0x91200
	s_lshl_b64 s[14:15], s[8:9], 1
	s_mul_i32 s16, s10, 0x810
	s_add_u32 s14, s57, s14
	s_addc_u32 s15, s58, s15
	s_lshl_b32 s17, s16, 1
	s_add_u32 s14, s14, s17
	s_addc_u32 s15, s15, 0
	s_lshl_b64 s[8:9], s[8:9], 2
	s_add_u32 s8, s59, s8
	s_addc_u32 s9, s60, s9
	s_lshl_b32 s16, s16, 2
	s_add_u32 s8, s8, s16
	v_mov_b32_e32 v9, v7
	s_addc_u32 s9, s9, 0
	v_lshl_add_u64 v[4:5], s[14:15], 0, v[8:9]
	v_or_b32_e32 v9, s10, v0
	v_mov_b32_e32 v95, 0
	v_lshl_add_u64 v[2:3], s[8:9], 0, v[6:7]
	s_mov_b32 s64, 0
	v_cmp_eq_u32_e64 s[8:9], 0, v9
	v_mov_b32_e32 v103, 0
	v_mov_b32_e32 v97, 0
	v_mov_b32_e32 v98, 0
	v_mov_b32_e32 v22, 0
	v_mov_b32_e32 v23, v95
	s_branch .LBB0_787
.LBB0_786:
	s_or_b64 exec, exec, s[14:15]
	v_add_f32_e32 v16, v23, v20
	v_max_f32_e32 v17, v21, v21
	v_max_f32_e32 v103, v16, v17
	v_sub_f32_e32 v16, v16, v103
	v_mul_f32_e32 v17, 0x3fb8aa3b, v16
	v_sub_f32_e32 v16, v21, v103
	v_mul_f32_e32 v16, 0x3fb8aa3b, v16
	v_exp_f32_e32 v16, v16
	v_exp_f32_e32 v18, v17
	s_add_i32 s10, s64, 18
	s_cmp_lt_u32 s64, 18
	v_mul_f32_e32 v97, v9, v16
	v_pk_mul_f32 v[10:11], v[10:11], v[16:17] op_sel_hi:[1,0]
	v_fmac_f32_e32 v97, v19, v18
	v_pk_fma_f32 v[22:23], v[12:13], v[18:19], v[10:11] op_sel_hi:[1,0,1]
	v_mov_b32_e32 v19, v16
	v_mul_f32_e32 v98, v30, v16
	v_pk_mul_f32 v[10:11], v[14:15], v[18:19]
	v_fmac_f32_e32 v98, v24, v18
	v_add_f32_e32 v95, v10, v11
	s_mov_b32 s64, s10
	s_cbranch_scc0 .LBB0_784

.LBB0_859:
	s_or_b64 exec, exec, s[28:29]
	s_lshl_b32 s28, s64, 2
	s_mov_b32 s29, s11
	s_lshl_b64 s[66:67], s[28:29], 2
	s_add_u32 s94, s62, s66
	s_addc_u32 s95, s63, s67
	s_waitcnt vmcnt(51)
	s_waitcnt vmcnt(48)
	s_waitcnt vmcnt(45)
	s_waitcnt vmcnt(42)
	s_waitcnt vmcnt(39)
	s_waitcnt vmcnt(36)
	s_waitcnt vmcnt(33)
	s_waitcnt vmcnt(30)
	s_waitcnt vmcnt(27)
	s_waitcnt vmcnt(24)
	s_waitcnt vmcnt(21)
	s_waitcnt vmcnt(18)
	s_waitcnt vmcnt(15)
	s_waitcnt vmcnt(12)
	s_waitcnt vmcnt(9)
	s_waitcnt vmcnt(6)
	s_waitcnt vmcnt(3)
	s_waitcnt vmcnt(0)
	s_sub_u32 s98, s94, s62
	s_lshr_b32 s98, s98, 4
	v_readlane_b32 s99, v249, s98
	v_readlane_b32 s98, v248, s98
	s_nop 1
	v_mov_b32_e32 v26, s98
	v_mov_b32_e32 v27, s99
	s_and_saveexec_b64 s[96:97], s[8:9]
	s_cbranch_execz .LBB0_861
	global_store_dword v7, v103, s[94:95] offset:8

.LBB0_865:
	s_or_b64 exec, exec, s[94:95]
	s_or_b32 s10, s28, 4
	s_lshl_b64 s[66:67], s[10:11], 2
	s_add_u32 s94, s62, s66
	v_add_f32_e32 v26, v103, v26
	v_max_f32_e32 v24, v27, v27
	s_addc_u32 s95, s63, s67
	v_max_f32_e32 v109, v26, v24
	s_sub_u32 s98, s94, s62
	s_lshr_b32 s98, s98, 4
	v_readlane_b32 s99, v249, s98
	v_readlane_b32 s98, v248, s98
	s_nop 1
	v_mov_b32_e32 v24, s98
	v_mov_b32_e32 v25, s99
	s_and_saveexec_b64 s[96:97], s[8:9]
	s_cbranch_execz .LBB0_867
	global_store_dword v7, v109, s[94:95] offset:8

.LBB0_871:
	s_or_b64 exec, exec, s[92:93]
	s_add_i32 s10, s28, 8
	s_lshl_b64 s[66:67], s[10:11], 2
	s_add_u32 s92, s62, s66
	v_add_f32_e32 v24, v109, v24
	v_max_f32_e32 v22, v25, v25
	s_addc_u32 s93, s63, s67
	v_max_f32_e32 v104, v24, v22
	s_sub_u32 s98, s92, s62
	s_lshr_b32 s98, s98, 4
	v_readlane_b32 s99, v249, s98
	v_readlane_b32 s98, v248, s98
	s_nop 1
	v_mov_b32_e32 v22, s98
	v_mov_b32_e32 v23, s99
	s_and_saveexec_b64 s[94:95], s[8:9]
	s_cbranch_execz .LBB0_873
	global_store_dword v7, v104, s[92:93] offset:8

.LBB0_877:
	s_or_b64 exec, exec, s[50:51]
	s_add_i32 s10, s28, 12
	s_lshl_b64 s[50:51], s[10:11], 2
	s_add_u32 s50, s62, s50
	v_add_f32_e32 v22, v104, v22
	v_max_f32_e32 v24, v23, v23
	s_addc_u32 s51, s63, s51
	v_max_f32_e32 v99, v22, v24
	s_sub_u32 s98, s50, s62
	s_lshr_b32 s98, s98, 4
	v_readlane_b32 s99, v249, s98
	v_readlane_b32 s98, v248, s98
	s_nop 1
	v_mov_b32_e32 v24, s98
	v_mov_b32_e32 v25, s99
	s_and_saveexec_b64 s[92:93], s[8:9]
	s_cbranch_execz .LBB0_879
	global_store_dword v7, v99, s[50:51] offset:8

.LBB0_883:
	s_or_b64 exec, exec, s[48:49]
	s_add_i32 s10, s28, 16
	s_lshl_b64 s[48:49], s[10:11], 2
	s_add_u32 s48, s62, s48
	v_add_f32_e32 v24, v99, v24
	v_max_f32_e32 v22, v25, v25
	s_addc_u32 s49, s63, s49
	v_max_f32_e32 v94, v24, v22
	s_sub_u32 s98, s48, s62
	s_lshr_b32 s98, s98, 4
	v_readlane_b32 s99, v249, s98
	v_readlane_b32 s98, v248, s98
	s_nop 1
	v_mov_b32_e32 v22, s98
	v_mov_b32_e32 v23, s99
	s_and_saveexec_b64 s[50:51], s[8:9]
	s_cbranch_execz .LBB0_885
	global_store_dword v7, v94, s[48:49] offset:8

.LBB0_889:
	s_or_b64 exec, exec, s[46:47]
	s_add_i32 s10, s28, 20
	s_lshl_b64 s[46:47], s[10:11], 2
	s_add_u32 s46, s62, s46
	v_add_f32_e32 v22, v94, v22
	v_max_f32_e32 v24, v23, v23
	s_addc_u32 s47, s63, s47
	v_max_f32_e32 v88, v22, v24
	s_sub_u32 s98, s46, s62
	s_lshr_b32 s98, s98, 4
	v_readlane_b32 s99, v249, s98
	v_readlane_b32 s98, v248, s98
	s_nop 1
	v_mov_b32_e32 v24, s98
	v_mov_b32_e32 v25, s99
	s_and_saveexec_b64 s[48:49], s[8:9]
	s_cbranch_execz .LBB0_891
	global_store_dword v7, v88, s[46:47] offset:8

.LBB0_895:
	s_or_b64 exec, exec, s[44:45]
	s_add_i32 s10, s28, 24
	s_lshl_b64 s[44:45], s[10:11], 2
	s_add_u32 s44, s62, s44
	v_add_f32_e32 v24, v88, v24
	v_max_f32_e32 v22, v25, v25
	s_addc_u32 s45, s63, s45
	v_max_f32_e32 v84, v24, v22
	s_sub_u32 s98, s44, s62
	s_lshr_b32 s98, s98, 4
	v_readlane_b32 s99, v249, s98
	v_readlane_b32 s98, v248, s98
	s_nop 1
	v_mov_b32_e32 v22, s98
	v_mov_b32_e32 v23, s99
	s_and_saveexec_b64 s[46:47], s[8:9]
	s_cbranch_execz .LBB0_897
	global_store_dword v7, v84, s[44:45] offset:8

.LBB0_901:
	s_or_b64 exec, exec, s[42:43]
	s_add_i32 s10, s28, 28
	s_lshl_b64 s[42:43], s[10:11], 2
	s_add_u32 s42, s62, s42
	v_add_f32_e32 v22, v84, v22
	v_max_f32_e32 v24, v23, v23
	s_addc_u32 s43, s63, s43
	v_max_f32_e32 v79, v22, v24
	s_sub_u32 s98, s42, s62
	s_lshr_b32 s98, s98, 4
	v_readlane_b32 s99, v249, s98
	v_readlane_b32 s98, v248, s98
	s_nop 1
	v_mov_b32_e32 v24, s98
	v_mov_b32_e32 v25, s99
	s_and_saveexec_b64 s[44:45], s[8:9]
	s_cbranch_execz .LBB0_903
	global_store_dword v7, v79, s[42:43] offset:8

.LBB0_907:
	s_or_b64 exec, exec, s[40:41]
	s_add_i32 s10, s28, 32
	s_lshl_b64 s[40:41], s[10:11], 2
	s_add_u32 s40, s62, s40
	v_add_f32_e32 v24, v79, v24
	v_max_f32_e32 v22, v25, v25
	s_addc_u32 s41, s63, s41
	v_max_f32_e32 v73, v24, v22
	s_sub_u32 s98, s40, s62
	s_lshr_b32 s98, s98, 4
	v_readlane_b32 s99, v249, s98
	v_readlane_b32 s98, v248, s98
	s_nop 1
	v_mov_b32_e32 v22, s98
	v_mov_b32_e32 v23, s99
	s_and_saveexec_b64 s[42:43], s[8:9]
	s_cbranch_execz .LBB0_909
	global_store_dword v7, v73, s[40:41] offset:8

.LBB0_913:
	s_or_b64 exec, exec, s[38:39]
	s_add_i32 s10, s28, 36
	s_lshl_b64 s[38:39], s[10:11], 2
	s_add_u32 s38, s62, s38
	v_add_f32_e32 v22, v73, v22
	v_max_f32_e32 v24, v23, v23
	s_addc_u32 s39, s63, s39
	v_max_f32_e32 v69, v22, v24
	s_sub_u32 s98, s38, s62
	s_lshr_b32 s98, s98, 4
	v_readlane_b32 s99, v249, s98
	v_readlane_b32 s98, v248, s98
	s_nop 1
	v_mov_b32_e32 v24, s98
	v_mov_b32_e32 v25, s99
	s_and_saveexec_b64 s[40:41], s[8:9]
	s_cbranch_execz .LBB0_915
	global_store_dword v7, v69, s[38:39] offset:8

.LBB0_919:
	s_or_b64 exec, exec, s[36:37]
	s_add_i32 s10, s28, 40
	s_lshl_b64 s[36:37], s[10:11], 2
	s_add_u32 s36, s62, s36
	v_add_f32_e32 v24, v69, v24
	v_max_f32_e32 v22, v25, v25
	s_addc_u32 s37, s63, s37
	v_max_f32_e32 v64, v24, v22
	s_sub_u32 s98, s36, s62
	s_lshr_b32 s98, s98, 4
	v_readlane_b32 s99, v249, s98
	v_readlane_b32 s98, v248, s98
	s_nop 1
	v_mov_b32_e32 v22, s98
	v_mov_b32_e32 v23, s99
	s_and_saveexec_b64 s[38:39], s[8:9]
	s_cbranch_execz .LBB0_921
	global_store_dword v7, v64, s[36:37] offset:8

.LBB0_925:
	s_or_b64 exec, exec, s[34:35]
	s_add_i32 s10, s28, 44
	s_lshl_b64 s[34:35], s[10:11], 2
	s_add_u32 s34, s62, s34
	v_add_f32_e32 v22, v64, v22
	v_max_f32_e32 v24, v23, v23
	s_addc_u32 s35, s63, s35
	v_max_f32_e32 v58, v22, v24
	s_sub_u32 s98, s34, s62
	s_lshr_b32 s98, s98, 4
	v_readlane_b32 s99, v249, s98
	v_readlane_b32 s98, v248, s98
	s_nop 1
	v_mov_b32_e32 v24, s98
	v_mov_b32_e32 v25, s99
	s_and_saveexec_b64 s[36:37], s[8:9]
	s_cbranch_execz .LBB0_927
	global_store_dword v7, v58, s[34:35] offset:8

.LBB0_931:
	s_or_b64 exec, exec, s[30:31]
	s_add_i32 s10, s28, 48
	s_lshl_b64 s[30:31], s[10:11], 2
	s_add_u32 s30, s62, s30
	s_addc_u32 s31, s63, s31
	s_sub_u32 s98, s30, s62
	s_lshr_b32 s98, s98, 4
	v_readlane_b32 s99, v249, s98
	v_readlane_b32 s98, v248, s98
	s_nop 1
	v_mov_b32_e32 v26, s98
	v_mov_b32_e32 v27, s99
	v_add_f32_e32 v22, v58, v24
	v_max_f32_e32 v23, v25, v25
	v_max_f32_e32 v54, v22, v23
	s_and_saveexec_b64 s[34:35], s[8:9]
	s_cbranch_execz .LBB0_933
	global_store_dword v7, v54, s[30:31] offset:8

.LBB0_937:
	s_or_b64 exec, exec, s[24:25]
	s_add_i32 s10, s28, 52
	s_lshl_b64 s[24:25], s[10:11], 2
	s_add_u32 s24, s62, s24
	v_add_f32_e32 v26, v54, v26
	v_max_f32_e32 v22, v27, v27
	s_addc_u32 s25, s63, s25
	v_max_f32_e32 v47, v26, v22
	s_sub_u32 s98, s24, s62
	s_lshr_b32 s98, s98, 4
	v_readlane_b32 s99, v249, s98
	v_readlane_b32 s98, v248, s98
	s_nop 1
	v_mov_b32_e32 v22, s98
	v_mov_b32_e32 v23, s99
	s_and_saveexec_b64 s[30:31], s[8:9]
	s_cbranch_execz .LBB0_939
	global_store_dword v7, v47, s[24:25] offset:8

.LBB0_943:
	s_or_b64 exec, exec, s[22:23]
	s_add_i32 s10, s28, 56
	s_lshl_b64 s[22:23], s[10:11], 2
	s_add_u32 s22, s62, s22
	s_addc_u32 s23, s63, s23
	s_sub_u32 s98, s22, s62
	s_lshr_b32 s98, s98, 4
	v_readlane_b32 s99, v249, s98
	v_readlane_b32 s98, v248, s98
	s_nop 1
	v_mov_b32_e32 v24, s98
	v_mov_b32_e32 v25, s99
	v_add_f32_e32 v14, v47, v22
	v_max_f32_e32 v22, v23, v23
	v_max_f32_e32 v44, v14, v22
	s_and_saveexec_b64 s[24:25], s[8:9]
	s_cbranch_execz .LBB0_945
	global_store_dword v7, v44, s[22:23] offset:8

.LBB0_949:
	s_or_b64 exec, exec, s[20:21]
	s_add_i32 s10, s28, 60
	s_lshl_b64 s[20:21], s[10:11], 2
	s_add_u32 s20, s62, s20
	v_add_f32_e32 v14, v44, v24
	v_max_f32_e32 v20, v25, v25
	s_addc_u32 s21, s63, s21
	v_max_f32_e32 v41, v14, v20
	s_sub_u32 s98, s20, s62
	s_lshr_b32 s98, s98, 4
	v_readlane_b32 s99, v249, s98
	v_readlane_b32 s98, v248, s98
	s_nop 1
	v_mov_b32_e32 v20, s98
	v_mov_b32_e32 v21, s99
	s_and_saveexec_b64 s[22:23], s[8:9]
	s_cbranch_execz .LBB0_951
	global_store_dword v7, v41, s[20:21] offset:8

.LBB0_955:
	s_or_b64 exec, exec, s[18:19]
	s_add_i32 s10, s28, 64
	s_lshl_b64 s[18:19], s[10:11], 2
	s_add_u32 s18, s62, s18
	v_add_f32_e32 v14, v41, v20
	v_max_f32_e32 v18, v21, v21
	s_addc_u32 s19, s63, s19
	v_max_f32_e32 v36, v14, v18
	s_sub_u32 s98, s18, s62
	s_lshr_b32 s98, s98, 4
	v_readlane_b32 s99, v249, s98
	v_readlane_b32 s98, v248, s98
	s_nop 1
	v_mov_b32_e32 v18, s98
	v_mov_b32_e32 v19, s99
	s_and_saveexec_b64 s[20:21], s[8:9]
	s_cbranch_execz .LBB0_957
	global_store_dword v7, v36, s[18:19] offset:8

.LBB0_961:
	s_or_b64 exec, exec, s[16:17]
	s_add_i32 s10, s28, 0x44
	s_lshl_b64 s[16:17], s[10:11], 2
	s_add_u32 s16, s62, s16
	s_addc_u32 s17, s63, s17
	s_sub_u32 s98, s16, s62
	s_lshr_b32 s98, s98, 4
	v_readlane_b32 s99, v249, s98
	v_readlane_b32 s98, v248, s98
	s_nop 1
	v_mov_b32_e32 v20, s98
	v_mov_b32_e32 v21, s99
	v_add_f32_e32 v14, v36, v18
	v_max_f32_e32 v18, v19, v19
	v_max_f32_e32 v23, v14, v18
	s_and_saveexec_b64 s[18:19], s[8:9]
	s_cbranch_execz .LBB0_963
	global_store_dword v7, v23, s[16:17] offset:8

.LBB0_2953:
	s_ashr_i32 s8, s67, 3
	s_and_b32 s10, s67, 7
	s_mul_i32 s14, s8, 0x240
	s_mul_hi_i32 s9, s8, 0x240
	s_add_u32 s68, s59, s14
	s_addc_u32 s69, s62, s9
	v_min_u32_e32 v250, 35, v164
	v_lshlrev_b32_e32 v250, 4, v250
	global_load_dwordx2 v[248:249], v250, s[68:69]
	s_mul_hi_i32 s9, s8, 0x91200
	s_mul_i32 s8, s8, 0x91200
	s_lshl_b64 s[14:15], s[8:9], 1
	s_mul_i32 s16, s10, 0x810
	s_add_u32 s14, s63, s14
	s_addc_u32 s15, s64, s15
	s_lshl_b32 s17, s16, 1
	s_add_u32 s14, s14, s17
	s_addc_u32 s15, s15, 0
	s_lshl_b64 s[8:9], s[8:9], 2
	s_add_u32 s8, s65, s8
	s_addc_u32 s9, s66, s9
	s_lshl_b32 s16, s16, 2
	s_add_u32 s8, s8, s16
	v_mov_b32_e32 v7, v169
	s_addc_u32 s9, s9, 0
	v_lshl_add_u64 v[4:5], s[14:15], 0, v[6:7]
	v_or_b32_e32 v7, s10, v0
	v_mov_b32_e32 v93, 0
	v_lshl_add_u64 v[2:3], s[8:9], 0, v[168:169]
	s_mov_b32 s70, 0
	v_cmp_eq_u32_e64 s[8:9], 0, v7
	v_mov_b32_e32 v101, 0
	v_mov_b32_e32 v95, 0
	v_mov_b32_e32 v96, 0
	v_mov_b32_e32 v20, 0
	v_mov_b32_e32 v21, v93
	s_branch .LBB0_2955
.LBB0_2954:
	s_or_b64 exec, exec, s[14:15]
	v_add_f32_e32 v14, v21, v18
	v_max_f32_e32 v15, v19, v19
	v_max_f32_e32 v101, v14, v15
	v_sub_f32_e32 v14, v14, v101
	v_mul_f32_e32 v15, 0x3fb8aa3b, v14
	v_sub_f32_e32 v14, v19, v101
	v_mul_f32_e32 v14, 0x3fb8aa3b, v14
	v_exp_f32_e32 v14, v14
	v_exp_f32_e32 v16, v15
	s_add_i32 s10, s70, 18
	s_cmp_lt_u32 s70, 18
	v_mul_f32_e32 v95, v7, v14
	v_pk_mul_f32 v[8:9], v[8:9], v[14:15] op_sel_hi:[1,0]
	v_fmac_f32_e32 v95, v17, v16
	v_pk_fma_f32 v[20:21], v[10:11], v[16:17], v[8:9] op_sel_hi:[1,0,1]
	v_mov_b32_e32 v17, v14
	v_mul_f32_e32 v96, v28, v14
	v_pk_mul_f32 v[8:9], v[12:13], v[16:17]
	v_fmac_f32_e32 v96, v22, v16
	v_add_f32_e32 v93, v8, v9
	s_mov_b32 s70, s10
	s_cbranch_scc0 .LBB0_2952

.LBB0_3027:
	s_or_b64 exec, exec, s[36:37]
	s_lshl_b32 s36, s70, 2
	s_mov_b32 s37, s11
	s_lshl_b64 s[56:57], s[36:37], 2
	s_add_u32 s56, s68, s56
	s_addc_u32 s57, s69, s57
	s_waitcnt vmcnt(51)
	s_waitcnt vmcnt(48)
	s_waitcnt vmcnt(45)
	s_waitcnt vmcnt(42)
	s_waitcnt vmcnt(39)
	s_waitcnt vmcnt(36)
	s_waitcnt vmcnt(33)
	s_waitcnt vmcnt(30)
	s_waitcnt vmcnt(27)
	s_waitcnt vmcnt(24)
	s_waitcnt vmcnt(21)
	s_waitcnt vmcnt(18)
	s_waitcnt vmcnt(15)
	s_waitcnt vmcnt(12)
	s_waitcnt vmcnt(9)
	s_waitcnt vmcnt(6)
	s_waitcnt vmcnt(3)
	s_waitcnt vmcnt(0)
	s_sub_u32 s98, s56, s68
	s_lshr_b32 s98, s98, 4
	v_readlane_b32 s99, v249, s98
	v_readlane_b32 s98, v248, s98
	s_nop 1
	v_mov_b32_e32 v24, s98
	v_mov_b32_e32 v25, s99
	s_and_saveexec_b64 s[60:61], s[8:9]
	s_cbranch_execz .LBB0_3029
	global_store_dword v169, v101, s[56:57] offset:8

.LBB0_3033:
	s_or_b64 exec, exec, s[56:57]
	s_or_b32 s10, s36, 4
	s_lshl_b64 s[56:57], s[10:11], 2
	s_add_u32 s56, s68, s56
	v_add_f32_e32 v24, v101, v24
	v_max_f32_e32 v22, v25, v25
	s_addc_u32 s57, s69, s57
	v_max_f32_e32 v107, v24, v22
	s_sub_u32 s98, s56, s68
	s_lshr_b32 s98, s98, 4
	v_readlane_b32 s99, v249, s98
	v_readlane_b32 s98, v248, s98
	s_nop 1
	v_mov_b32_e32 v22, s98
	v_mov_b32_e32 v23, s99
	s_and_saveexec_b64 s[60:61], s[8:9]
	s_cbranch_execz .LBB0_3035
	global_store_dword v169, v107, s[56:57] offset:8

.LBB0_3039:
	s_or_b64 exec, exec, s[54:55]
	s_add_i32 s10, s36, 8
	s_lshl_b64 s[54:55], s[10:11], 2
	s_add_u32 s54, s68, s54
	v_add_f32_e32 v22, v107, v22
	v_max_f32_e32 v20, v23, v23
	s_addc_u32 s55, s69, s55
	v_max_f32_e32 v102, v22, v20
	s_sub_u32 s98, s54, s68
	s_lshr_b32 s98, s98, 4
	v_readlane_b32 s99, v249, s98
	v_readlane_b32 s98, v248, s98
	s_nop 1
	v_mov_b32_e32 v20, s98
	v_mov_b32_e32 v21, s99
	s_and_saveexec_b64 s[56:57], s[8:9]
	s_cbranch_execz .LBB0_3041
	global_store_dword v169, v102, s[54:55] offset:8

.LBB0_3045:
	s_or_b64 exec, exec, s[50:51]
	s_add_i32 s10, s36, 12
	s_lshl_b64 s[50:51], s[10:11], 2
	s_add_u32 s50, s68, s50
	v_add_f32_e32 v20, v102, v20
	v_max_f32_e32 v22, v21, v21
	s_addc_u32 s51, s69, s51
	v_max_f32_e32 v97, v20, v22
	s_sub_u32 s98, s50, s68
	s_lshr_b32 s98, s98, 4
	v_readlane_b32 s99, v249, s98
	v_readlane_b32 s98, v248, s98
	s_nop 1
	v_mov_b32_e32 v22, s98
	v_mov_b32_e32 v23, s99
	s_and_saveexec_b64 s[54:55], s[8:9]
	s_cbranch_execz .LBB0_3047
	global_store_dword v169, v97, s[50:51] offset:8

.LBB0_3051:
	s_or_b64 exec, exec, s[48:49]
	s_add_i32 s10, s36, 16
	s_lshl_b64 s[48:49], s[10:11], 2
	s_add_u32 s48, s68, s48
	v_add_f32_e32 v22, v97, v22
	v_max_f32_e32 v20, v23, v23
	s_addc_u32 s49, s69, s49
	v_max_f32_e32 v92, v22, v20
	s_sub_u32 s98, s48, s68
	s_lshr_b32 s98, s98, 4
	v_readlane_b32 s99, v249, s98
	v_readlane_b32 s98, v248, s98
	s_nop 1
	v_mov_b32_e32 v20, s98
	v_mov_b32_e32 v21, s99
	s_and_saveexec_b64 s[50:51], s[8:9]
	s_cbranch_execz .LBB0_3053
	global_store_dword v169, v92, s[48:49] offset:8

.LBB0_3057:
	s_or_b64 exec, exec, s[46:47]
	s_add_i32 s10, s36, 20
	s_lshl_b64 s[46:47], s[10:11], 2
	s_add_u32 s46, s68, s46
	v_add_f32_e32 v20, v92, v20
	v_max_f32_e32 v22, v21, v21
	s_addc_u32 s47, s69, s47
	v_max_f32_e32 v86, v20, v22
	s_sub_u32 s98, s46, s68
	s_lshr_b32 s98, s98, 4
	v_readlane_b32 s99, v249, s98
	v_readlane_b32 s98, v248, s98
	s_nop 1
	v_mov_b32_e32 v22, s98
	v_mov_b32_e32 v23, s99
	s_and_saveexec_b64 s[48:49], s[8:9]
	s_cbranch_execz .LBB0_3059
	global_store_dword v169, v86, s[46:47] offset:8

.LBB0_3063:
	s_or_b64 exec, exec, s[44:45]
	s_add_i32 s10, s36, 24
	s_lshl_b64 s[44:45], s[10:11], 2
	s_add_u32 s44, s68, s44
	v_add_f32_e32 v22, v86, v22
	v_max_f32_e32 v20, v23, v23
	s_addc_u32 s45, s69, s45
	v_max_f32_e32 v82, v22, v20
	s_sub_u32 s98, s44, s68
	s_lshr_b32 s98, s98, 4
	v_readlane_b32 s99, v249, s98
	v_readlane_b32 s98, v248, s98
	s_nop 1
	v_mov_b32_e32 v20, s98
	v_mov_b32_e32 v21, s99
	s_and_saveexec_b64 s[46:47], s[8:9]
	s_cbranch_execz .LBB0_3065
	global_store_dword v169, v82, s[44:45] offset:8

.LBB0_3069:
	s_or_b64 exec, exec, s[42:43]
	s_add_i32 s10, s36, 28
	s_lshl_b64 s[42:43], s[10:11], 2
	s_add_u32 s42, s68, s42
	v_add_f32_e32 v20, v82, v20
	v_max_f32_e32 v22, v21, v21
	s_addc_u32 s43, s69, s43
	v_max_f32_e32 v24, v20, v22
	s_sub_u32 s98, s42, s68
	s_lshr_b32 s98, s98, 4
	v_readlane_b32 s99, v249, s98
	v_readlane_b32 s98, v248, s98
	s_nop 1
	v_mov_b32_e32 v22, s98
	v_mov_b32_e32 v23, s99
	s_and_saveexec_b64 s[44:45], s[8:9]
	s_cbranch_execz .LBB0_3071
	global_store_dword v169, v24, s[42:43] offset:8

.LBB0_3075:
	s_or_b64 exec, exec, s[40:41]
	s_add_i32 s10, s36, 32
	s_lshl_b64 s[40:41], s[10:11], 2
	s_add_u32 s40, s68, s40
	v_add_f32_e32 v22, v24, v22
	v_max_f32_e32 v20, v23, v23
	s_addc_u32 s41, s69, s41
	v_max_f32_e32 v24, v22, v20
	s_sub_u32 s98, s40, s68
	s_lshr_b32 s98, s98, 4
	v_readlane_b32 s99, v249, s98
	v_readlane_b32 s98, v248, s98
	s_nop 1
	v_mov_b32_e32 v20, s98
	v_mov_b32_e32 v21, s99
	s_and_saveexec_b64 s[42:43], s[8:9]
	s_cbranch_execz .LBB0_3077
	global_store_dword v169, v24, s[40:41] offset:8

.LBB0_3081:
	s_or_b64 exec, exec, s[38:39]
	s_add_i32 s10, s36, 36
	s_lshl_b64 s[38:39], s[10:11], 2
	s_add_u32 s38, s68, s38
	s_addc_u32 s39, s69, s39
	s_sub_u32 s98, s38, s68
	s_lshr_b32 s98, s98, 4
	v_readlane_b32 s99, v249, s98
	v_readlane_b32 s98, v248, s98
	s_nop 1
	v_mov_b32_e32 v22, s98
	v_mov_b32_e32 v23, s99
	v_add_f32_e32 v20, v24, v20
	v_max_f32_e32 v24, v21, v21
	v_max_f32_e32 v67, v20, v24
	s_and_saveexec_b64 s[40:41], s[8:9]
	s_cbranch_execz .LBB0_3083
	global_store_dword v169, v67, s[38:39] offset:8

.LBB0_3087:
	s_or_b64 exec, exec, s[34:35]
	s_add_i32 s10, s36, 40
	s_lshl_b64 s[34:35], s[10:11], 2
	s_add_u32 s34, s68, s34
	s_addc_u32 s35, s69, s35
	s_sub_u32 s98, s34, s68
	s_lshr_b32 s98, s98, 4
	v_readlane_b32 s99, v249, s98
	v_readlane_b32 s98, v248, s98
	s_nop 1
	v_mov_b32_e32 v20, s98
	v_mov_b32_e32 v21, s99
	v_add_f32_e32 v22, v67, v22
	v_max_f32_e32 v61, v23, v23
	v_max_f32_e32 v61, v22, v61
	s_and_saveexec_b64 s[38:39], s[8:9]
	s_cbranch_execz .LBB0_3089
	global_store_dword v169, v61, s[34:35] offset:8

.LBB0_3093:
	s_or_b64 exec, exec, s[30:31]
	s_add_i32 s10, s36, 44
	s_lshl_b64 s[30:31], s[10:11], 2
	s_add_u32 s30, s68, s30
	s_addc_u32 s31, s69, s31
	s_sub_u32 s98, s30, s68
	s_lshr_b32 s98, s98, 4
	v_readlane_b32 s99, v249, s98
	v_readlane_b32 s98, v248, s98
	s_nop 1
	v_mov_b32_e32 v22, s98
	v_mov_b32_e32 v23, s99
	v_add_f32_e32 v20, v61, v20
	v_max_f32_e32 v25, v21, v21
	v_max_f32_e32 v57, v20, v25
	s_and_saveexec_b64 s[34:35], s[8:9]
	s_cbranch_execz .LBB0_3095
	global_store_dword v169, v57, s[30:31] offset:8

.LBB0_3099:
	s_or_b64 exec, exec, s[28:29]
	s_add_i32 s10, s36, 48
	s_lshl_b64 s[28:29], s[10:11], 2
	s_add_u32 s28, s68, s28
	s_addc_u32 s29, s69, s29
	s_sub_u32 s98, s28, s68
	s_lshr_b32 s98, s98, 4
	v_readlane_b32 s99, v249, s98
	v_readlane_b32 s98, v248, s98
	s_nop 1
	v_mov_b32_e32 v24, s98
	v_mov_b32_e32 v25, s99
	v_add_f32_e32 v20, v57, v22
	v_max_f32_e32 v21, v23, v23
	v_max_f32_e32 v52, v20, v21
	s_and_saveexec_b64 s[30:31], s[8:9]
	s_cbranch_execz .LBB0_3101
	global_store_dword v169, v52, s[28:29] offset:8

.LBB0_3105:
	s_or_b64 exec, exec, s[24:25]
	s_add_i32 s10, s36, 52
	s_lshl_b64 s[24:25], s[10:11], 2
	s_add_u32 s24, s68, s24
	s_addc_u32 s25, s69, s25
	s_sub_u32 s98, s24, s68
	s_lshr_b32 s98, s98, 4
	v_readlane_b32 s99, v249, s98
	v_readlane_b32 s98, v248, s98
	s_nop 1
	v_mov_b32_e32 v20, s98
	v_mov_b32_e32 v21, s99
	v_add_f32_e32 v24, v52, v24
	v_max_f32_e32 v44, v25, v25
	v_max_f32_e32 v45, v24, v44
	s_and_saveexec_b64 s[28:29], s[8:9]
	s_cbranch_execz .LBB0_3107
	global_store_dword v169, v45, s[24:25] offset:8

.LBB0_3111:
	s_or_b64 exec, exec, s[22:23]
	s_add_i32 s10, s36, 56
	s_lshl_b64 s[22:23], s[10:11], 2
	s_add_u32 s22, s68, s22
	s_addc_u32 s23, s69, s23
	s_sub_u32 s98, s22, s68
	s_lshr_b32 s98, s98, 4
	v_readlane_b32 s99, v249, s98
	v_readlane_b32 s98, v248, s98
	s_nop 1
	v_mov_b32_e32 v22, s98
	v_mov_b32_e32 v23, s99
	v_add_f32_e32 v12, v45, v20
	v_max_f32_e32 v20, v21, v21
	v_max_f32_e32 v42, v12, v20
	s_and_saveexec_b64 s[24:25], s[8:9]
	s_cbranch_execz .LBB0_3113
	global_store_dword v169, v42, s[22:23] offset:8

.LBB0_3117:
	s_or_b64 exec, exec, s[20:21]
	s_add_i32 s10, s36, 60
	s_lshl_b64 s[20:21], s[10:11], 2
	s_add_u32 s20, s68, s20
	s_addc_u32 s21, s69, s21
	s_sub_u32 s98, s20, s68
	s_lshr_b32 s98, s98, 4
	v_readlane_b32 s99, v249, s98
	v_readlane_b32 s98, v248, s98
	s_nop 1
	v_mov_b32_e32 v18, s98
	v_mov_b32_e32 v19, s99
	v_add_f32_e32 v12, v42, v22
	v_max_f32_e32 v22, v23, v23
	v_max_f32_e32 v39, v12, v22
	s_and_saveexec_b64 s[22:23], s[8:9]
	s_cbranch_execz .LBB0_3119
	global_store_dword v169, v39, s[20:21] offset:8

.LBB0_3123:
	s_or_b64 exec, exec, s[18:19]
	s_add_i32 s10, s36, 64
	s_lshl_b64 s[18:19], s[10:11], 2
	s_add_u32 s18, s68, s18
	s_addc_u32 s19, s69, s19
	s_sub_u32 s98, s18, s68
	s_lshr_b32 s98, s98, 4
	v_readlane_b32 s99, v249, s98
	v_readlane_b32 s98, v248, s98
	s_nop 1
	v_mov_b32_e32 v16, s98
	v_mov_b32_e32 v17, s99
	v_add_f32_e32 v12, v39, v18
	v_max_f32_e32 v18, v19, v19
	v_max_f32_e32 v34, v12, v18
	s_and_saveexec_b64 s[20:21], s[8:9]
	s_cbranch_execz .LBB0_3125
	global_store_dword v169, v34, s[18:19] offset:8

.LBB0_3129:
	s_or_b64 exec, exec, s[16:17]
	s_add_i32 s10, s36, 0x44
	s_lshl_b64 s[16:17], s[10:11], 2
	s_add_u32 s16, s68, s16
	s_addc_u32 s17, s69, s17
	s_sub_u32 s98, s16, s68
	s_lshr_b32 s98, s98, 4
	v_readlane_b32 s99, v249, s98
	v_readlane_b32 s98, v248, s98
	s_nop 1
	v_mov_b32_e32 v18, s98
	v_mov_b32_e32 v19, s99
	v_add_f32_e32 v12, v34, v16
	v_max_f32_e32 v16, v17, v17
	v_max_f32_e32 v21, v12, v16
	s_and_saveexec_b64 s[18:19], s[8:9]
	s_cbranch_execz .LBB0_3131
	global_store_dword v169, v21, s[16:17] offset:8

	.amdhsa_kernel _Z10fwd_kernel4Args
		.amdhsa_group_segment_fixed_size 0
		.amdhsa_private_segment_fixed_size 0
		.amdhsa_kernarg_size 568
		.amdhsa_user_sgpr_count 2
		.amdhsa_user_sgpr_dispatch_ptr 0
		.amdhsa_user_sgpr_queue_ptr 0
		.amdhsa_user_sgpr_kernarg_segment_ptr 1
		.amdhsa_user_sgpr_dispatch_id 0
		.amdhsa_user_sgpr_kernarg_preload_length 0
		.amdhsa_user_sgpr_kernarg_preload_offset 0
		.amdhsa_user_sgpr_private_segment_size 0
		.amdhsa_uses_dynamic_stack 0
		.amdhsa_enable_private_segment 0
		.amdhsa_system_sgpr_workgroup_id_x 1
		.amdhsa_system_sgpr_workgroup_id_y 0
		.amdhsa_system_sgpr_workgroup_id_z 0
		.amdhsa_system_sgpr_workgroup_info 0
		.amdhsa_system_vgpr_workitem_id 0
		.amdhsa_next_free_vgpr 256
		.amdhsa_next_free_sgpr 100
		.amdhsa_accum_offset 256
		.amdhsa_reserve_vcc 1
		.amdhsa_float_round_mode_32 0
		.amdhsa_float_round_mode_16_64 0
		.amdhsa_float_denorm_mode_32 3
		.amdhsa_float_denorm_mode_16_64 3
		.amdhsa_dx10_clamp 1
		.amdhsa_ieee_mode 1
		.amdhsa_fp16_overflow 0
		.amdhsa_tg_split 0
		.amdhsa_exception_fp_ieee_invalid_op 0
		.amdhsa_exception_fp_denorm_src 0
		.amdhsa_exception_fp_ieee_div_zero 0
		.amdhsa_exception_fp_ieee_overflow 0
		.amdhsa_exception_fp_ieee_underflow 0
		.amdhsa_exception_fp_ieee_inexact 0
		.amdhsa_exception_int_div_zero 0
	.end_amdhsa_kernel

amdhsa.kernels:
  - .agpr_count:     0
    .args:
      - .offset:         0
        .size:           312
        .value_kind:     by_value
      - .offset:         312
        .size:           4
        .value_kind:     hidden_block_count_x
      - .offset:         316
        .size:           4
        .value_kind:     hidden_block_count_y
      - .offset:         320
        .size:           4
        .value_kind:     hidden_block_count_z
      - .offset:         324
        .size:           2
        .value_kind:     hidden_group_size_x
      - .offset:         326
        .size:           2
        .value_kind:     hidden_group_size_y
      - .offset:         328
        .size:           2
        .value_kind:     hidden_group_size_z
      - .offset:         330
        .size:           2
        .value_kind:     hidden_remainder_x
      - .offset:         332
        .size:           2
        .value_kind:     hidden_remainder_y
      - .offset:         334
        .size:           2
        .value_kind:     hidden_remainder_z
      - .offset:         352
        .size:           8
        .value_kind:     hidden_global_offset_x
      - .offset:         360
        .size:           8
        .value_kind:     hidden_global_offset_y
      - .offset:         368
        .size:           8
        .value_kind:     hidden_global_offset_z
      - .offset:         376
        .size:           2
        .value_kind:     hidden_grid_dims
      - .offset:         432
        .size:           4
        .value_kind:     hidden_dynamic_lds_size
    .group_segment_fixed_size: 0
    .kernarg_segment_align: 8
    .kernarg_segment_size: 568
    .language:       OpenCL C
    .language_version:
      - 2
      - 0
    .max_flat_workgroup_size: 512
    .name:           _Z10fwd_kernel4Args
    .private_segment_fixed_size: 0
    .sgpr_count:     106
    .sgpr_spill_count: 83
    .symbol:         _Z10fwd_kernel4Args.kd
    .uniform_work_group_size: 1
    .uses_dynamic_stack: false
    .vgpr_count:     256
    .vgpr_spill_count: 0
    .wavefront_size: 64
